# speedup vs baseline: 1.0020x; 1.0020x over previous
.LBB3_2:
	v_add_u32_e32 v206, s27, v214
	ds_read_b64_tr_b16 v[194:195], v206 offset:24576
	ds_read_b64_tr_b16 v[196:197], v206 offset:25088
	s_waitcnt lgkmcnt(9)
	v_mfma_f32_32x32x16_bf16 v[114:129], v[190:193], v[158:161], v[50:65]
	v_add_f32_e32 v98, v82, v83
	v_add_f32_e32 v98, v84, v98
	v_add_f32_e32 v98, v85, v98
	v_add_f32_e32 v98, v86, v98
	v_add_f32_e32 v130, v87, v98
	v_cvt_pk_bf16_f32 v142, v82, v83
	v_cvt_pk_bf16_f32 v143, v84, v85
	ds_read_b64_tr_b16 v[190:191], v206 offset:28672
	ds_read_b64_tr_b16 v[192:193], v206 offset:29184
	v_add_f32_e32 v82, v88, v130
	v_add_f32_e32 v82, v89, v82
	s_waitcnt lgkmcnt(10)
	v_mfma_f32_32x32x16_bf16 v[98:113], v[186:189], v[158:161], v[50:65]
	v_add_f32_e32 v82, v90, v82
	v_add_f32_e32 v82, v91, v82
	v_cvt_pk_bf16_f32 v144, v86, v87
	v_cvt_pk_bf16_f32 v145, v88, v89
	ds_read_b64_tr_b16 v[186:187], v206 offset:25600
	ds_read_b64_tr_b16 v[188:189], v206 offset:26112
	s_waitcnt lgkmcnt(11)
	v_mfma_f32_32x32x16_bf16 v[114:129], v[182:185], v[154:157], v[114:129]
	v_add_f32_e32 v82, v92, v82
	v_add_f32_e32 v82, v93, v82
	v_add_f32_e32 v82, v94, v82
	v_add_f32_e32 v82, v95, v82
	v_cvt_pk_bf16_f32 v138, v90, v91
	v_cvt_pk_bf16_f32 v139, v92, v93
	ds_read_b64_tr_b16 v[86:87], v206 offset:29696
	ds_read_b64_tr_b16 v[88:89], v206 offset:30208
	s_waitcnt lgkmcnt(12)
	v_mfma_f32_32x32x16_bf16 v[98:113], v[178:181], v[154:157], v[98:113]
	v_add_f32_e32 v82, v96, v82
	v_add_f32_e32 v82, v97, v82
	v_add_f32_e32 v82, v66, v82
	v_add_f32_e32 v90, v67, v82
	v_cvt_pk_bf16_f32 v140, v94, v95
	v_cvt_pk_bf16_f32 v141, v96, v97
	ds_read_b64_tr_b16 v[82:83], v206 offset:26624
	ds_read_b64_tr_b16 v[84:85], v206 offset:27136
	s_waitcnt lgkmcnt(13)
	v_mfma_f32_32x32x16_bf16 v[114:129], v[174:177], v[150:153], v[114:129]
	v_add_f32_e32 v90, v68, v90
	v_add_f32_e32 v90, v69, v90
	v_add_f32_e32 v90, v70, v90
	v_add_f32_e32 v90, v71, v90
	v_cvt_pk_bf16_f32 v134, v66, v67
	v_cvt_pk_bf16_f32 v135, v68, v69
	ds_read_b64_tr_b16 v[66:67], v206 offset:30720
	ds_read_b64_tr_b16 v[68:69], v206 offset:31232
	s_waitcnt lgkmcnt(14)
	v_mfma_f32_32x32x16_bf16 v[98:113], v[170:173], v[150:153], v[98:113]
	v_add_f32_e32 v90, v72, v90
	v_add_f32_e32 v90, v73, v90
	v_add_f32_e32 v90, v74, v90
	v_add_f32_e32 v90, v75, v90
	v_cvt_pk_bf16_f32 v136, v70, v71
	v_cvt_pk_bf16_f32 v137, v72, v73
	ds_read_b64_tr_b16 v[70:71], v206 offset:27648
	ds_read_b64_tr_b16 v[72:73], v206 offset:28160
	s_waitcnt lgkmcnt(14)
	v_mfma_f32_32x32x16_bf16 v[114:129], v[166:169], v[146:149], v[114:129]
	v_add_f32_e32 v90, v76, v90
	v_add_f32_e32 v90, v77, v90
	v_add_f32_e32 v90, v78, v90
	v_add_f32_e32 v90, v79, v90
	v_cvt_pk_bf16_f32 v130, v74, v75
	v_cvt_pk_bf16_f32 v131, v76, v77
	ds_read_b64_tr_b16 v[74:75], v206 offset:31744
	ds_read_b64_tr_b16 v[76:77], v206 offset:32256
	v_mfma_f32_32x32x16_bf16 v[98:113], v[162:165], v[146:149], v[98:113]
	v_add_f32_e32 v90, v80, v90
	v_add_f32_e32 v90, v81, v90
	v_cvt_pk_bf16_f32 v132, v78, v79
	v_cvt_pk_bf16_f32 v133, v80, v81
	s_nop 0
	v_lshl_add_u64 v[78:79], v[204:205], 0, s[24:25]
	s_add_i32 s26, s39, s35
	s_mov_b32 m0, s26
	s_nop 0
	global_load_lds_dwordx4 v[78:79], off
	v_max_f32_e32 v78, v114, v115
	s_nop 2
	v_max3_f32 v79, v116, v117, v99
	v_max3_f32 v78, v78, v98, v100
	v_max3_f32 v78, v78, v101, v118
	v_max3_f32 v79, v79, v120, v121
	v_max3_f32 v78, v78, v119, v102
	v_max3_f32 v79, v79, v104, v105
	v_max3_f32 v78, v78, v103, v122
	v_max3_f32 v79, v79, v124, v125
	v_max3_f32 v78, v78, v123, v106
	v_max3_f32 v79, v79, v108, v109
	v_max3_f32 v78, v78, v107, v126
	v_max3_f32 v79, v79, v128, v129
	v_max3_f32 v78, v78, v127, v110
	v_max3_f32 v79, v79, v112, v113
	v_max3_f32 v78, v78, v111, v79
	v_mov_b32_e32 v79, v78
	s_nop 1
	v_permlane32_swap_b32_e32 v78, v79
	v_max_f32_e32 v78, v78, v79
	v_lshl_add_u64 v[206:207], v[208:209], 0, s[18:19]
	s_add_i32 s26, s38, s34
	s_mov_b32 m0, s26
	s_nop 0
	global_load_lds_dwordx4 v[206:207], off
	v_cmp_lt_f32_e32 vcc, s15, v78
	s_cmp_lg_u64 vcc, 0
	v_add_f32_e32 v201, v201, v90
	s_cselect_b64 s[26:27], -1, 0
	s_cbranch_vccnz .LBB3_11

.LBB3_6:
	s_add_i32 s26, s38, 0x2000
	s_cmpk_lg_i32 s38, 0x4000
	s_cselect_b32 s40, s26, 0
	v_add_u32_e32 v217, s39, v214
	ds_read_b64_tr_b16 v[162:163], v217 offset:24576
	ds_read_b64_tr_b16 v[164:165], v217 offset:25088
	s_waitcnt lgkmcnt(9)
	v_mfma_f32_32x32x16_bf16 v[82:97], v[78:81], v[158:161], v[50:65]
	v_add_f32_e32 v66, v114, v115
	v_add_f32_e32 v66, v116, v66
	v_add_f32_e32 v66, v117, v66
	v_add_f32_e32 v66, v118, v66
	v_add_f32_e32 v66, v119, v66
	v_cvt_pk_bf16_f32 v142, v114, v115
	v_cvt_pk_bf16_f32 v143, v116, v117
	ds_read_b64_tr_b16 v[170:171], v217 offset:28672
	ds_read_b64_tr_b16 v[172:173], v217 offset:29184
	v_add_f32_e32 v66, v120, v66
	v_add_f32_e32 v66, v121, v66
	v_add_f32_e32 v66, v122, v66
	v_add_f32_e32 v114, v123, v66
	s_waitcnt lgkmcnt(10)
	v_mfma_f32_32x32x16_bf16 v[66:81], v[166:169], v[158:161], v[50:65]
	v_cvt_pk_bf16_f32 v144, v118, v119
	v_cvt_pk_bf16_f32 v145, v120, v121
	ds_read_b64_tr_b16 v[166:167], v217 offset:25600
	ds_read_b64_tr_b16 v[168:169], v217 offset:26112
	s_waitcnt lgkmcnt(11)
	v_mfma_f32_32x32x16_bf16 v[82:97], v[194:197], v[154:157], v[82:97]
	v_add_f32_e32 v114, v124, v114
	v_add_f32_e32 v114, v125, v114
	v_add_f32_e32 v114, v126, v114
	v_add_f32_e32 v114, v127, v114
	v_cvt_pk_bf16_f32 v138, v122, v123
	v_cvt_pk_bf16_f32 v139, v124, v125
	ds_read_b64_tr_b16 v[118:119], v217 offset:29696
	ds_read_b64_tr_b16 v[120:121], v217 offset:30208
	s_waitcnt lgkmcnt(12)
	v_mfma_f32_32x32x16_bf16 v[66:81], v[190:193], v[154:157], v[66:81]
	v_add_f32_e32 v114, v128, v114
	v_add_f32_e32 v114, v129, v114
	v_add_f32_e32 v114, v98, v114
	v_add_f32_e32 v122, v99, v114
	v_cvt_pk_bf16_f32 v140, v126, v127
	v_cvt_pk_bf16_f32 v141, v128, v129
	ds_read_b64_tr_b16 v[114:115], v217 offset:26624
	ds_read_b64_tr_b16 v[116:117], v217 offset:27136
	s_waitcnt lgkmcnt(13)
	v_mfma_f32_32x32x16_bf16 v[82:97], v[186:189], v[150:153], v[82:97]
	v_add_f32_e32 v122, v100, v122
	v_add_f32_e32 v122, v101, v122
	v_add_f32_e32 v122, v102, v122
	v_add_f32_e32 v122, v103, v122
	v_cvt_pk_bf16_f32 v134, v98, v99
	v_cvt_pk_bf16_f32 v135, v100, v101
	ds_read_b64_tr_b16 v[98:99], v217 offset:30720
	ds_read_b64_tr_b16 v[100:101], v217 offset:31232
	s_waitcnt lgkmcnt(14)
	v_mfma_f32_32x32x16_bf16 v[66:81], v[178:181], v[150:153], v[66:81]
	v_add_f32_e32 v122, v104, v122
	v_add_f32_e32 v122, v105, v122
	v_add_f32_e32 v122, v106, v122
	v_add_f32_e32 v122, v107, v122
	v_cvt_pk_bf16_f32 v136, v102, v103
	v_cvt_pk_bf16_f32 v137, v104, v105
	ds_read_b64_tr_b16 v[102:103], v217 offset:27648
	ds_read_b64_tr_b16 v[104:105], v217 offset:28160
	s_waitcnt lgkmcnt(14)
	v_mfma_f32_32x32x16_bf16 v[82:97], v[182:185], v[146:149], v[82:97]
	v_add_f32_e32 v122, v108, v122
	v_add_f32_e32 v122, v109, v122
	v_add_f32_e32 v122, v110, v122
	v_add_f32_e32 v122, v111, v122
	v_cvt_pk_bf16_f32 v130, v106, v107
	v_cvt_pk_bf16_f32 v131, v108, v109
	ds_read_b64_tr_b16 v[106:107], v217 offset:31744
	ds_read_b64_tr_b16 v[108:109], v217 offset:32256
	v_mfma_f32_32x32x16_bf16 v[66:81], v[174:177], v[146:149], v[66:81]
	v_add_f32_e32 v122, v112, v122
	v_add_f32_e32 v122, v113, v122
	v_cvt_pk_bf16_f32 v132, v110, v111
	v_cvt_pk_bf16_f32 v133, v112, v113
	s_nop 0
	v_lshl_add_u64 v[110:111], v[204:205], 0, s[20:21]
	s_add_i32 s26, s38, s35
	s_mov_b32 m0, s26
	s_nop 0
	global_load_lds_dwordx4 v[110:111], off
	v_lshl_add_u64 v[110:111], v[208:209], 0, s[16:17]
	s_add_i32 s26, s40, s34
	s_mov_b32 m0, s26
	s_nop 0
	global_load_lds_dwordx4 v[110:111], off
	v_max_f32_e32 v110, v82, v83
	s_nop 0
	v_max3_f32 v111, v84, v85, v67
	v_max3_f32 v110, v110, v66, v68
	v_max3_f32 v110, v110, v69, v86
	v_max3_f32 v111, v111, v88, v89
	v_max3_f32 v110, v110, v87, v70
	v_max3_f32 v111, v111, v72, v73
	v_max3_f32 v110, v110, v71, v90
	v_max3_f32 v111, v111, v92, v93
	v_max3_f32 v110, v110, v91, v74
	v_max3_f32 v111, v111, v76, v77
	v_max3_f32 v110, v110, v75, v94
	v_max3_f32 v111, v111, v96, v97
	v_max3_f32 v110, v110, v95, v78
	v_max3_f32 v111, v111, v80, v81
	v_max3_f32 v110, v110, v79, v111
	v_mov_b32_e32 v111, v110
	s_nop 1
	v_permlane32_swap_b32_e32 v110, v111
	v_max_f32_e32 v110, v110, v111
	v_cmp_lt_f32_e32 vcc, s15, v110
	s_cmp_lg_u64 vcc, 0
	v_add_f32_e32 v201, v201, v122
	s_cselect_b64 s[26:27], -1, 0
	s_cbranch_vccnz .LBB3_14
